# helper share 4x171 runs
# speedup vs baseline: 1.0137x; 1.0137x over previous
; #define LDS_AS __attribute__((address_space(3)))
; #define OPAQUE_TID(P) (((P).wid0 << 6) | lane_id_now())
; template <int NS, bool STREAM_ONLY = false>
; DI void convert_experts_dma(const Params& p, LDS_AS unsigned char* lds, int bid, int nb) {
;   const int tid = OPAQUE_TID(p), wid = __builtin_amdgcn_readfirstlane(tid >> 6), lane = tid & 63;
;   constexpr int NT = 32 * 1536;
;   const int nvalid = bid < NT / CVG ? CVG * ((NT / CVG - bid + nb - 1) / nb) : 0;
; __global__ void __launch_bounds__(NTHREADS, 2) k_forward(Params p_in) {
;     ...
;     if (ncv == 0) convert_experts_dma<4>(p, lds, bid, nb);
.LBB0_1119:
	s_or_b64 exec, exec, s[0:1]
	s_mov_b64 s[12:13], 0
	s_mov_b32 s20, 0
	s_mov_b64 s[0:1], 0
	v_readlane_b32 s97, v255, 13
	s_mov_b32 s99, s96
	s_nop 0
	s_mov_b32 s98, s97
	s_cmp_lg_u32 s55, 0
	s_cbranch_scc0 .LBB0_1181
	v_readlane_b32 s98, v255, 17
	s_sub_i32 s99, s96, s55
	s_add_i32 s98, s98, 0x2d54
	s_branch .LBB0_1181
.LBB0_1121:
	v_mov_b32_e32 v0, 0
	ds_read_b32 v2, v0
	ds_read_b32 v3, v0 offset:4
	s_waitcnt lgkmcnt(0)
	s_barrier
	v_mbcnt_lo_u32_b32 v0, -1, 0
	v_mbcnt_hi_u32_b32 v0, -1, v0
	s_mov_b32 s6, 0
	v_or_b32_e32 v1, s87, v0
	s_cmpk_gt_i32 s54, 0x2d53
	v_readfirstlane_b32 s0, v1
	s_mov_b32 s18, 0
	s_cbranch_scc1 .LBB0_1123
	s_abs_i32 s1, s55
	v_cvt_f32_u32_e32 v1, s1
	s_sub_i32 s2, s55, s54
	s_add_i32 s3, s2, 0x2d53
	s_sub_i32 s2, 0xffffd2ad, s2
	v_rcp_iflag_f32_e32 v1, v1
	s_xor_b32 s5, s3, s55
	s_sub_i32 s4, 0, s1
	s_max_i32 s2, s3, s2
	v_mul_f32_e32 v1, 0x4f7ffffe, v1
	v_cvt_u32_f32_e32 v1, v1
	s_ashr_i32 s3, s5, 31
	v_readfirstlane_b32 s5, v1
	s_mul_i32 s4, s4, s5
	s_mul_hi_u32 s4, s5, s4
	s_add_i32 s5, s5, s4
	s_mul_hi_u32 s4, s2, s5
	s_mul_i32 s5, s4, s1
	s_sub_i32 s2, s2, s5
	s_add_i32 s7, s4, 1
	s_sub_i32 s5, s2, s1
	s_cmp_ge_u32 s2, s1
	s_cselect_b32 s4, s7, s4
	s_cselect_b32 s2, s5, s2
	s_add_i32 s5, s4, 1
	s_cmp_ge_u32 s2, s1
	s_cselect_b32 s1, s5, s4
	s_xor_b32 s1, s1, s3
	s_sub_i32 s1, s1, s3
	s_lshl_b32 s18, s1, 2
